# DPP quad_perm instead of ds_bpermute for the lane^1 exchanges of the gate|up rstd table build (6 per phase) and the phase A |q|_1 sum
# speedup vs baseline: 1.0085x; 1.0085x over previous
; __device__ __forceinline__ unsigned long long rt() { return __builtin_amdgcn_s_memrealtime(); }
; __global__ void __launch_bounds__(NWAVES * 64, 2) mk_fwd(Args args) {
;     ...
;                     for (int i = 0; i < 6; ++i) { ok[i] = S.next(i, uu[i]); const int pm_ = ok[i] ? uu[i].pm : 0, pn_ = ok[i] ? uu[i].pn : 0;
;                         const f32x4* p = (const f32x4*)(W_ss + ((size_t)pm_ * 256 + (ftid >> 1)) * 32 + (ftid & 1) * 16);
;                         sv[i][0] = p[0]; sv[i][1] = p[1]; sv[i][2] = p[2]; sv[i][3] = p[3];
;                         bv[i] = bias[pn_ * 256 + (ftid & 255)]; }
;                     __syncthreads();
; #pragma unroll
;                     for (int i = 0; i < 6; ++i) { const f32x4 t4 = (sv[i][0] + sv[i][1]) + (sv[i][2] + sv[i][3]); float s1 = (t4[0] + t4[1]) + (t4[2] + t4[3]); s1 += __shfl_xor(s1, 1);
;                         if ((ftid & 1) == 0) rt[i * 256 + (ftid >> 1)] = __builtin_amdgcn_rsqf(s1 * (1.0f / D) + EPS);
;                         if (ftid < 256) bt[i * 256 + ftid] = bv[i]; }
.LBB0_213:
	v_mov_b64_e32 v[82:83], 0x580
	v_cmp_lt_i64_e32 vcc, s[4:5], v[82:83]
	s_lshl_b32 s6, s39, 8
	s_and_b64 s[4:5], vcc, exec
	v_lshl_add_u64 v[82:83], s[2:3], 0, v[96:97]
	s_cselect_b32 s4, s6, 0
	v_lshlrev_b64 v[82:83], 7, v[82:83]
	v_lshl_add_u64 v[92:93], v[80:81], 0, v[82:83]
	v_or_b32_sdwa v106, s4, v99 dst_sel:DWORD dst_unused:UNUSED_PAD src0_sel:DWORD src1_sel:BYTE_0
	global_load_dwordx4 v[80:83], v[92:93], off offset:48
	global_load_dwordx4 v[84:87], v[92:93], off offset:32
	global_load_dwordx4 v[88:91], v[92:93], off offset:16
	s_nop 0
	global_load_dwordx4 v[92:95], v[92:93], off
	v_ashrrev_i32_e32 v107, 31, v106
	v_lshl_add_u64 v[106:107], v[106:107], 2, s[30:31]
	global_load_dword v97, v[106:107], off
	v_and_b32_e32 v106, 64, v228
	v_xor_b32_e32 v105, 1, v228
	v_add_u32_e32 v106, 64, v106
	s_waitcnt vmcnt(26)
	v_pk_add_f32 v[10:11], v[14:15], v[10:11]
	v_pk_add_f32 v[8:9], v[12:13], v[8:9]
	v_pk_add_f32 v[0:1], v[4:5], v[0:1]
	v_pk_add_f32 v[2:3], v[6:7], v[2:3]
	v_cmp_lt_i32_e32 vcc, v105, v106
	v_pk_add_f32 v[2:3], v[10:11], v[2:3]
	v_pk_add_f32 v[0:1], v[8:9], v[0:1]
	v_cndmask_b32_e32 v105, v228, v105, vcc
	v_add_f32_e32 v0, v0, v1
	v_add_f32_e32 v1, v2, v3
	v_lshlrev_b32_e32 v105, 2, v105
	v_add_f32_e32 v1, v0, v1
	s_nop 1
	v_mov_b32_dpp v2, v1 quad_perm:[1,0,3,2] row_mask:0xf bank_mask:0xf
	v_and_b32_e32 v0, 1, v98
	s_add_i32 s2, 0, 0x22000
	v_cmp_eq_u32_e32 vcc, 0, v0
	v_lshl_add_u32 v0, v96, 2, s2
	s_waitcnt lgkmcnt(0)
	s_barrier
	s_and_saveexec_b64 s[2:3], vcc
	s_cbranch_execz .LBB0_215
	v_add_f32_e32 v1, v1, v2
	v_fmamk_f32 v1, v1, 0x3a000000, v229
	v_rsq_f32_e32 v1, v1
	ds_write_b32 v0, v1

; __device__ __forceinline__ unsigned long long rt() { return __builtin_amdgcn_s_memrealtime(); }
; __global__ void __launch_bounds__(NWAVES * 64, 2) mk_fwd(Args args) {
;     ...
;                     for (int i = 0; i < 6; ++i) { const f32x4 t4 = (sv[i][0] + sv[i][1]) + (sv[i][2] + sv[i][3]); float s1 = (t4[0] + t4[1]) + (t4[2] + t4[3]); s1 += __shfl_xor(s1, 1);
;                         if ((ftid & 1) == 0) rt[i * 256 + (ftid >> 1)] = __builtin_amdgcn_rsqf(s1 * (1.0f / D) + EPS);
;                         if (ftid < 256) bt[i * 256 + ftid] = bv[i]; }
.LBB0_217:
	s_or_b64 exec, exec, s[4:5]
	s_waitcnt vmcnt(21)
	v_pk_add_f32 v[2:3], v[30:31], v[26:27]
	v_pk_add_f32 v[4:5], v[28:29], v[24:25]
	v_pk_add_f32 v[6:7], v[20:21], v[16:17]
	v_pk_add_f32 v[8:9], v[22:23], v[18:19]
	v_pk_add_f32 v[4:5], v[4:5], v[6:7]
	v_pk_add_f32 v[2:3], v[2:3], v[8:9]
	v_add_f32_e32 v4, v4, v5
	v_add_f32_e32 v2, v2, v3
	v_add_f32_e32 v2, v4, v2
	s_nop 1
	v_mov_b32_dpp v3, v2 quad_perm:[1,0,3,2] row_mask:0xf bank_mask:0xf
	s_and_saveexec_b64 s[4:5], vcc
	s_cbranch_execz .LBB0_219
	s_waitcnt lgkmcnt(0)
	v_add_f32_e32 v2, v2, v3
	v_fmamk_f32 v2, v2, 0x3a000000, v229
	v_rsq_f32_e32 v2, v2
	ds_write_b32 v0, v2 offset:1024

; __device__ __forceinline__ unsigned long long rt() { return __builtin_amdgcn_s_memrealtime(); }
; __global__ void __launch_bounds__(NWAVES * 64, 2) mk_fwd(Args args) {
;     ...
;                     for (int i = 0; i < 6; ++i) { const f32x4 t4 = (sv[i][0] + sv[i][1]) + (sv[i][2] + sv[i][3]); float s1 = (t4[0] + t4[1]) + (t4[2] + t4[3]); s1 += __shfl_xor(s1, 1);
;                         if ((ftid & 1) == 0) rt[i * 256 + (ftid >> 1)] = __builtin_amdgcn_rsqf(s1 * (1.0f / D) + EPS);
;                         if (ftid < 256) bt[i * 256 + ftid] = bv[i]; }
.LBB0_221:
	s_or_b64 exec, exec, s[4:5]
	s_waitcnt vmcnt(16) lgkmcnt(0)
	v_pk_add_f32 v[2:3], v[46:47], v[42:43]
	v_pk_add_f32 v[4:5], v[44:45], v[40:41]
	v_pk_add_f32 v[6:7], v[36:37], v[32:33]
	v_pk_add_f32 v[8:9], v[38:39], v[34:35]
	v_pk_add_f32 v[4:5], v[4:5], v[6:7]
	v_pk_add_f32 v[2:3], v[2:3], v[8:9]
	v_add_f32_e32 v4, v4, v5
	v_add_f32_e32 v2, v2, v3
	v_add_f32_e32 v2, v4, v2
	s_nop 1
	v_mov_b32_dpp v3, v2 quad_perm:[1,0,3,2] row_mask:0xf bank_mask:0xf
	s_and_saveexec_b64 s[4:5], vcc
	s_cbranch_execz .LBB0_223
	s_waitcnt lgkmcnt(0)
	v_add_f32_e32 v2, v2, v3
	v_fmamk_f32 v2, v2, 0x3a000000, v229
	v_rsq_f32_e32 v2, v2
	ds_write_b32 v0, v2 offset:2048

; __device__ __forceinline__ unsigned long long rt() { return __builtin_amdgcn_s_memrealtime(); }
; __global__ void __launch_bounds__(NWAVES * 64, 2) mk_fwd(Args args) {
;     ...
;                     for (int i = 0; i < 6; ++i) { const f32x4 t4 = (sv[i][0] + sv[i][1]) + (sv[i][2] + sv[i][3]); float s1 = (t4[0] + t4[1]) + (t4[2] + t4[3]); s1 += __shfl_xor(s1, 1);
;                         if ((ftid & 1) == 0) rt[i * 256 + (ftid >> 1)] = __builtin_amdgcn_rsqf(s1 * (1.0f / D) + EPS);
;                         if (ftid < 256) bt[i * 256 + ftid] = bv[i]; }
.LBB0_225:
	s_or_b64 exec, exec, s[4:5]
	s_waitcnt vmcnt(11) lgkmcnt(0)
	v_pk_add_f32 v[2:3], v[62:63], v[58:59]
	v_pk_add_f32 v[4:5], v[60:61], v[56:57]
	v_pk_add_f32 v[6:7], v[52:53], v[48:49]
	v_pk_add_f32 v[8:9], v[54:55], v[50:51]
	v_pk_add_f32 v[4:5], v[4:5], v[6:7]
	v_pk_add_f32 v[2:3], v[2:3], v[8:9]
	v_add_f32_e32 v4, v4, v5
	v_add_f32_e32 v2, v2, v3
	v_add_f32_e32 v2, v4, v2
	s_nop 1
	v_mov_b32_dpp v3, v2 quad_perm:[1,0,3,2] row_mask:0xf bank_mask:0xf
	s_and_saveexec_b64 s[4:5], vcc
	s_cbranch_execz .LBB0_227
	s_waitcnt lgkmcnt(0)
	v_add_f32_e32 v2, v2, v3
	v_fmamk_f32 v2, v2, 0x3a000000, v229
	v_rsq_f32_e32 v2, v2
	ds_write_b32 v0, v2 offset:3072

; __device__ __forceinline__ unsigned long long rt() { return __builtin_amdgcn_s_memrealtime(); }
; __global__ void __launch_bounds__(NWAVES * 64, 2) mk_fwd(Args args) {
;     ...
;                     for (int i = 0; i < 6; ++i) { const f32x4 t4 = (sv[i][0] + sv[i][1]) + (sv[i][2] + sv[i][3]); float s1 = (t4[0] + t4[1]) + (t4[2] + t4[3]); s1 += __shfl_xor(s1, 1);
;                         if ((ftid & 1) == 0) rt[i * 256 + (ftid >> 1)] = __builtin_amdgcn_rsqf(s1 * (1.0f / D) + EPS);
;                         if (ftid < 256) bt[i * 256 + ftid] = bv[i]; }
.LBB0_229:
	s_or_b64 exec, exec, s[4:5]
	s_waitcnt vmcnt(6) lgkmcnt(0)
	v_pk_add_f32 v[2:3], v[78:79], v[74:75]
	v_pk_add_f32 v[4:5], v[76:77], v[72:73]
	v_pk_add_f32 v[6:7], v[68:69], v[64:65]
	v_pk_add_f32 v[8:9], v[70:71], v[66:67]
	v_pk_add_f32 v[4:5], v[4:5], v[6:7]
	v_pk_add_f32 v[2:3], v[2:3], v[8:9]
	v_add_f32_e32 v4, v4, v5
	v_add_f32_e32 v2, v2, v3
	v_add_f32_e32 v2, v4, v2
	s_nop 1
	v_mov_b32_dpp v3, v2 quad_perm:[1,0,3,2] row_mask:0xf bank_mask:0xf
	s_and_saveexec_b64 s[4:5], vcc
	s_cbranch_execz .LBB0_231
	s_waitcnt lgkmcnt(0)
	v_add_f32_e32 v2, v2, v3
	v_fmamk_f32 v2, v2, 0x3a000000, v229
	v_rsq_f32_e32 v2, v2
	ds_write_b32 v0, v2 offset:4096

; __device__ __forceinline__ unsigned long long rt() { return __builtin_amdgcn_s_memrealtime(); }
; __global__ void __launch_bounds__(NWAVES * 64, 2) mk_fwd(Args args) {
;     ...
;                     for (int i = 0; i < 6; ++i) { const f32x4 t4 = (sv[i][0] + sv[i][1]) + (sv[i][2] + sv[i][3]); float s1 = (t4[0] + t4[1]) + (t4[2] + t4[3]); s1 += __shfl_xor(s1, 1);
;                         if ((ftid & 1) == 0) rt[i * 256 + (ftid >> 1)] = __builtin_amdgcn_rsqf(s1 * (1.0f / D) + EPS);
;                         if (ftid < 256) bt[i * 256 + ftid] = bv[i]; }
.LBB0_233:
	s_or_b64 exec, exec, s[4:5]
	s_waitcnt vmcnt(1) lgkmcnt(0)
	v_pk_add_f32 v[2:3], v[94:95], v[90:91]
	v_pk_add_f32 v[4:5], v[92:93], v[88:89]
	v_pk_add_f32 v[6:7], v[84:85], v[80:81]
	v_pk_add_f32 v[8:9], v[86:87], v[82:83]
	v_pk_add_f32 v[4:5], v[4:5], v[6:7]
	v_pk_add_f32 v[2:3], v[2:3], v[8:9]
	v_add_f32_e32 v4, v4, v5
	v_add_f32_e32 v2, v2, v3
	v_add_f32_e32 v2, v4, v2
	s_nop 1
	v_mov_b32_dpp v3, v2 quad_perm:[1,0,3,2] row_mask:0xf bank_mask:0xf
	s_and_saveexec_b64 s[4:5], vcc
	s_cbranch_execz .LBB0_235
	s_waitcnt lgkmcnt(0)
	v_add_f32_e32 v2, v2, v3
	v_fmamk_f32 v2, v2, 0x3a000000, v229
	v_rsq_f32_e32 v2, v2
	ds_write_b32 v0, v2 offset:5120

; __global__ void __launch_bounds__(NWAVES * 64, 2) mk_fwd(Args args) {
;     ...
;                             float l1 = 0.f;
; #pragma unroll
;                             for (int i = 0; i < 64; ++i) l1 += fabsf(q[i]);
;                             l1 += __shfl_xor(l1, 1);
;                             const float kmaxv = __uint_as_float(__hip_atomic_load(W_ctl + 12288 + j * 64 + h_, __ATOMIC_RELAXED, __HIP_MEMORY_SCOPE_AGENT));
;                             const float Bq = mb::SCALE * l1 * kmaxv * 1.02f, slope = exp2f(-(float)(h_ + 1) * 0.5f);
;                             const float Dz = (2.f * Bq + 104.f) / slope, posf = (float)(qb_ * 256 + row - 255);
;                             if (i0 >= 0 && posf - (float)(i0 * 256) > Dz) i0 = -1;
;                             if (i1 >= 0 && posf - (float)(i1 * 256) > Dz) i1 = -1;
;                             if (i2 >= 0 && posf - (float)(i2 * 256) > Dz) i2 = -1;
;                         }
.Lpa_done:
	v_add_f32_e64 v10, |v10|, |v11|
	v_add_f32_e64 v10, v10, |v12|
	v_add_f32_e64 v10, v10, |v13|
	v_add_f32_e64 v10, v10, |v14|
	v_add_f32_e64 v10, v10, |v15|
	v_add_f32_e64 v10, v10, |v16|
	v_add_f32_e64 v10, v10, |v17|
	v_add_f32_e64 v10, v10, |v18|
	v_add_f32_e64 v10, v10, |v19|
	v_add_f32_e64 v10, v10, |v20|
	v_add_f32_e64 v10, v10, |v21|
	v_add_f32_e64 v10, v10, |v22|
	v_add_f32_e64 v10, v10, |v23|
	v_add_f32_e64 v10, v10, |v24|
	v_add_f32_e64 v10, v10, |v25|
	v_add_f32_e64 v10, v10, |v26|
	v_add_f32_e64 v10, v10, |v27|
	v_add_f32_e64 v10, v10, |v28|
	v_add_f32_e64 v10, v10, |v29|
	v_add_f32_e64 v10, v10, |v30|
	v_add_f32_e64 v10, v10, |v31|
	v_add_f32_e64 v10, v10, |v32|
	v_add_f32_e64 v10, v10, |v33|
	v_add_f32_e64 v10, v10, |v34|
	v_add_f32_e64 v10, v10, |v35|
	v_add_f32_e64 v10, v10, |v36|
	v_add_f32_e64 v10, v10, |v37|
	v_add_f32_e64 v10, v10, |v38|
	v_add_f32_e64 v10, v10, |v39|
	v_add_f32_e64 v10, v10, |v40|
	v_add_f32_e64 v10, v10, |v41|
	v_add_f32_e64 v10, v10, |v42|
	v_add_f32_e64 v10, v10, |v43|
	v_add_f32_e64 v10, v10, |v44|
	v_add_f32_e64 v10, v10, |v45|
	v_add_f32_e64 v10, v10, |v46|
	v_add_f32_e64 v10, v10, |v47|
	v_add_f32_e64 v10, v10, |v48|
	v_add_f32_e64 v10, v10, |v49|
	v_add_f32_e64 v10, v10, |v50|
	v_add_f32_e64 v10, v10, |v51|
	v_add_f32_e64 v10, v10, |v52|
	v_add_f32_e64 v10, v10, |v53|
	v_add_f32_e64 v10, v10, |v54|
	v_add_f32_e64 v10, v10, |v55|
	v_add_f32_e64 v10, v10, |v56|
	v_add_f32_e64 v10, v10, |v57|
	v_add_f32_e64 v10, v10, |v58|
	v_add_f32_e64 v10, v10, |v59|
	v_add_f32_e64 v10, v10, |v60|
	v_add_f32_e64 v10, v10, |v61|
	v_add_f32_e64 v10, v10, |v62|
	v_add_f32_e64 v10, v10, |v63|
	v_add_f32_e64 v10, v10, |v64|
	v_add_f32_e64 v10, v10, |v65|
	v_add_f32_e64 v10, v10, |v66|
	v_add_f32_e64 v10, v10, |v67|
	v_add_f32_e64 v10, v10, |v68|
	v_add_f32_e64 v10, v10, |v69|
	v_add_f32_e64 v10, v10, |v70|
	v_add_f32_e64 v10, v10, |v71|
	v_add_f32_e64 v10, v10, |v72|
	v_add_f32_e64 v10, v10, |v73|
	s_nop 1
	v_mov_b32_dpp v11, v10 quad_perm:[1,0,3,2] row_mask:0xf bank_mask:0xf
	s_waitcnt lgkmcnt(0)
	v_add_f32_e32 v10, v10, v11
	v_mul_f32_e32 v10, 0x3db504f3, v10
	s_waitcnt vmcnt(0)
	v_mul_f32_e32 v10, v10, v137
	v_mul_f32_e32 v10, 0x3f828f5c, v10
	v_fmaak_f32 v10, 2.0, v10, 0x42d00000
	v_div_scale_f32 v11, s[12:13], v82, v82, v10
	v_rcp_f32_e32 v12, v11
	s_nop 0
	v_fma_f32 v13, -v11, v12, 1.0
	v_fmac_f32_e32 v12, v13, v12
	v_div_scale_f32 v13, vcc, v10, v82, v10
	v_mul_f32_e32 v14, v13, v12
	v_fma_f32 v15, -v11, v14, v13
	v_fmac_f32_e32 v14, v15, v12
	v_fma_f32 v11, -v11, v14, v13
	v_div_fmas_f32 v11, v11, v12, v14
	v_div_fixup_f32 v10, v11, v82, v10
	v_add_u32_e32 v11, s64, v77
	v_cvt_f32_i32_e32 v11, v11
	v_cmp_lt_i32_e32 vcc, -1, v85
	s_and_saveexec_b64 s[12:13], vcc
	s_cbranch_execz .LBB0_587
	v_lshlrev_b32_e32 v12, 8, v85
	v_cvt_f32_u32_e32 v12, v12
	v_sub_f32_e32 v12, v11, v12
	v_cmp_gt_f32_e32 vcc, v12, v10
	s_and_saveexec_b64 s[14:15], vcc
	v_mov_b32_e32 v85, -1
	s_or_b64 exec, exec, s[14:15]
	s_or_b64 exec, exec, s[12:13]
	v_cmp_lt_i32_e32 vcc, -1, v84
	s_and_saveexec_b64 s[12:13], vcc
	s_cbranch_execnz .LBB0_588
